# v067 + packed->plain f32 in router phase P6 (209 sites)
# baseline (speedup 1.0000x reference)
; #define P6_LD(bi, r) do { const GAS f32x4* xr_ = (const GAS f32x4*)(XOUT + ((size_t)p * 256 + wave * 32 + (r)) * DM) + lane2; _Pragma("unroll") for (int j = 0; j < 4; ++j) xq[bi][j] = xr_[64 * j]; } while (0)
; __device__ __forceinline__ unsigned f2bf(float f) { unsigned u = __builtin_bit_cast(unsigned, f); return (u + 0x7fffu + ((u >> 16) & 1u)) >> 16; }
; __device__ __forceinline__ unsigned pk2(float lo, float hi) { return f2bf(lo) | (f2bf(hi) << 16); }
; __global__ void __launch_bounds__(512, 2) hymba_fwd(Args args) {
;     ...
;             { f32x4 av[4], sv[4]; int lane2 = lane; asm volatile("" : "+v"(lane2));
; #pragma unroll
;               for (int j = 0; j < 4; ++j) { const int c0 = 4 * lane2 + 256 * j; sv[j] = *(const f32x4*)(sh2 + c0); av[j] = *(const f32x4*)(g2p + c0) * (1.0f + *(const f32x4*)(scl2 + c0)); }
;               f32x4 xq[4][4];
;     ...
;               P6_LD(0, 0); P6_LD(1, 1); P6_LD(2, 2); asm volatile("" ::: "memory");
; #pragma nounroll
;               for (int rr = 0; rr < 32; rr += 4) { const int r4 = (rr + 4 < 32) ? rr + 4 : 28;
;                   P6_LD(3, rr + 3); asm volatile("" ::: "memory"); P6_ST(0, rr); asm volatile("" ::: "memory");
;                   P6_LD(0, r4); asm volatile("" ::: "memory"); P6_ST(1, rr + 1); asm volatile("" ::: "memory");
;                   P6_LD(1, r4 + 1); asm volatile("" ::: "memory"); P6_ST(2, rr + 2); asm volatile("" ::: "memory");
;                   P6_LD(2, r4 + 2); asm volatile("" ::: "memory"); P6_ST(3, rr + 3); asm volatile("" ::: "memory"); }
.LBB0_877:
	s_add_i32 s43, s16, 3
	s_add_i32 s17, s16, 4
	s_cmp_lt_u32 s16, 28
	s_cselect_b32 s10, s17, 28
	s_add_u32 s8, s2, s10
	s_addc_u32 s9, s3, 0
	s_lshl_b64 s[14:15], s[8:9], 12
	s_add_i32 s59, s16, 1
	s_or_b32 s8, s10, 1
	s_add_u32 s8, s2, s8
	s_addc_u32 s9, s3, 0
	s_lshl_b64 s[12:13], s[8:9], 12
	s_add_i32 s58, s16, 2
	s_or_b32 s8, s10, 2
	s_add_u32 s8, s2, s8
	s_addc_u32 s9, s3, 0
	s_lshl_b64 s[10:11], s[8:9], 12
	s_add_u32 s8, s18, 0x2000
	s_addc_u32 s9, s19, 0
	s_cmp_gt_u32 s16, 27
	v_readlane_b32 s16, v80, s16
	v_lshl_add_u64 v[104:105], s[18:19], 0, v[100:101]
	s_movk_i32 s18, 0xf000
	s_waitcnt vmcnt(11)
	v_mul_f32_e32 v48, s16, v48
	v_mul_f32_e32 v49, s16, v49
	v_fma_f32 v48, v48, v84, v0
	v_fma_f32 v49, v49, v85, v1
	v_mul_f32_e32 v50, s16, v50
	v_mul_f32_e32 v51, s16, v51
	v_bfe_u32 v81, v48, 16, 1
	v_add3_u32 v48, v48, v81, s23
	v_bfe_u32 v81, v49, 16, 1
	v_fma_f32 v50, v50, v82, v2
	v_fma_f32 v51, v51, v83, v3
	v_lshrrev_b32_e32 v48, 16, v48
	v_add3_u32 v49, v49, v81, s23
	v_and_or_b32 v48, v49, s42, v48
	v_bfe_u32 v49, v50, 16, 1
	v_add3_u32 v49, v50, v49, s23
	v_bfe_u32 v50, v51, 16, 1
	v_lshrrev_b32_e32 v49, 16, v49
	v_add3_u32 v50, v51, v50, s23
	v_add_co_u32_e32 v106, vcc, s18, v104
	s_waitcnt vmcnt(10)
	v_mul_f32_e32 v36, s16, v36
	v_mul_f32_e32 v37, s16, v37
	v_and_or_b32 v49, v50, s42, v49
	v_addc_co_u32_e32 v107, vcc, -1, v105, vcc
	v_fma_f32 v36, v36, v88, v4
	v_fma_f32 v37, v37, v89, v5
	global_load_dwordx4 v[76:79], v[102:103], off
	global_load_dwordx4 v[72:75], v[102:103], off offset:1024
	global_load_dwordx4 v[68:71], v[102:103], off offset:2048
	global_load_dwordx4 v[64:67], v[102:103], off offset:3072
	global_store_dwordx2 v[106:107], v[48:49], off offset:-3584
	v_bfe_u32 v48, v36, 16, 1
	v_mul_f32_e32 v38, s16, v38
	v_mul_f32_e32 v39, s16, v39
	v_add3_u32 v36, v36, v48, s23
	v_bfe_u32 v48, v37, 16, 1
	v_fma_f32 v38, v38, v86, v6
	v_fma_f32 v39, v39, v87, v7
	v_lshrrev_b32_e32 v36, 16, v36
	v_add3_u32 v37, v37, v48, s23
	v_and_or_b32 v36, v37, s42, v36
	v_bfe_u32 v37, v38, 16, 1
	v_add3_u32 v37, v38, v37, s23
	v_bfe_u32 v38, v39, 16, 1
	v_lshrrev_b32_e32 v37, 16, v37
	v_add3_u32 v38, v39, v38, s23
	s_waitcnt vmcnt(14)
	v_mul_f32_e32 v28, s16, v28
	v_mul_f32_e32 v29, s16, v29
	v_and_or_b32 v37, v38, s42, v37
	v_fma_f32 v28, v28, v92, v8
	v_fma_f32 v29, v29, v93, v9
	global_store_dwordx2 v[106:107], v[36:37], off offset:-3072
	v_bfe_u32 v36, v28, 16, 1
	v_mul_f32_e32 v30, s16, v30
	v_mul_f32_e32 v31, s16, v31
	v_add3_u32 v28, v28, v36, s23
	v_bfe_u32 v36, v29, 16, 1
	v_fma_f32 v30, v30, v90, v10
	v_fma_f32 v31, v31, v91, v11
	v_lshrrev_b32_e32 v28, 16, v28
	v_add3_u32 v29, v29, v36, s23
	v_and_or_b32 v28, v29, s42, v28
	v_bfe_u32 v29, v30, 16, 1
	v_add3_u32 v29, v30, v29, s23
	v_bfe_u32 v30, v31, 16, 1
	v_lshrrev_b32_e32 v29, 16, v29
	v_add3_u32 v30, v31, v30, s23
	s_waitcnt vmcnt(14)
	v_mul_f32_e32 v20, s16, v20
	v_mul_f32_e32 v21, s16, v21
	v_and_or_b32 v29, v30, s42, v29
	v_fma_f32 v20, v20, v96, v12
	v_fma_f32 v21, v21, v97, v13
	global_store_dwordx2 v[106:107], v[28:29], off offset:-2560
	v_bfe_u32 v28, v20, 16, 1
	v_mul_f32_e32 v22, s16, v22
	v_mul_f32_e32 v23, s16, v23
	v_add3_u32 v20, v20, v28, s23
	v_bfe_u32 v28, v21, 16, 1
	v_fma_f32 v22, v22, v94, v14
	v_fma_f32 v23, v23, v95, v15
	v_lshrrev_b32_e32 v20, 16, v20
	v_add3_u32 v21, v21, v28, s23
	v_and_or_b32 v20, v21, s42, v20
	v_bfe_u32 v21, v22, 16, 1
	v_add3_u32 v21, v22, v21, s23
	v_bfe_u32 v22, v23, 16, 1
	v_lshrrev_b32_e32 v21, 16, v21
	v_add3_u32 v22, v23, v22, s23
	v_and_or_b32 v21, v22, s42, v21
	global_store_dwordx2 v[106:107], v[20:21], off offset:-2048
	v_lshl_add_u64 v[20:21], v[98:99], 0, s[14:15]
	v_readlane_b32 s14, v80, s59
	global_load_dwordx4 v[48:51], v[20:21], off
	global_load_dwordx4 v[36:39], v[20:21], off offset:1024
	global_load_dwordx4 v[28:31], v[20:21], off offset:2048
	s_nop 0
	global_load_dwordx4 v[20:23], v[20:21], off offset:3072
	s_waitcnt vmcnt(19)
	v_mul_f32_e32 v40, s14, v40
	v_mul_f32_e32 v41, s14, v41
	v_fma_f32 v40, v40, v84, v0
	v_fma_f32 v41, v41, v85, v1
	v_mul_f32_e32 v42, s14, v42
	v_mul_f32_e32 v43, s14, v43
	v_bfe_u32 v81, v40, 16, 1
	v_add3_u32 v40, v40, v81, s23
	v_bfe_u32 v81, v41, 16, 1
	v_fma_f32 v42, v42, v82, v2
	v_fma_f32 v43, v43, v83, v3
	v_lshrrev_b32_e32 v40, 16, v40
	v_add3_u32 v41, v41, v81, s23
	v_and_or_b32 v40, v41, s42, v40
	v_bfe_u32 v41, v42, 16, 1
	v_add3_u32 v41, v42, v41, s23
	v_bfe_u32 v42, v43, 16, 1
	v_lshrrev_b32_e32 v41, 16, v41
	v_add3_u32 v42, v43, v42, s23
	s_waitcnt vmcnt(18)
	v_mul_f32_e32 v32, s14, v32
	v_mul_f32_e32 v33, s14, v33
	v_and_or_b32 v41, v42, s42, v41
	v_fma_f32 v32, v32, v88, v4
	v_fma_f32 v33, v33, v89, v5
	global_store_dwordx2 v[106:107], v[40:41], off offset:-1536
	v_bfe_u32 v40, v32, 16, 1
	v_mul_f32_e32 v34, s14, v34
	v_mul_f32_e32 v35, s14, v35
	v_add3_u32 v32, v32, v40, s23
	v_bfe_u32 v40, v33, 16, 1
	v_fma_f32 v34, v34, v86, v6
	v_fma_f32 v35, v35, v87, v7
	v_lshrrev_b32_e32 v32, 16, v32
	v_add3_u32 v33, v33, v40, s23
	v_and_or_b32 v32, v33, s42, v32
	v_bfe_u32 v33, v34, 16, 1
	v_add3_u32 v33, v34, v33, s23
	v_bfe_u32 v34, v35, 16, 1
	v_lshrrev_b32_e32 v33, 16, v33
	v_add3_u32 v34, v35, v34, s23
	s_waitcnt vmcnt(18)
	v_mul_f32_e32 v24, s14, v24
	v_mul_f32_e32 v25, s14, v25
	v_and_or_b32 v33, v34, s42, v33
	v_fma_f32 v24, v24, v92, v8
	v_fma_f32 v25, v25, v93, v9
	global_store_dwordx2 v[106:107], v[32:33], off offset:-1024
	v_bfe_u32 v32, v24, 16, 1
	v_mul_f32_e32 v26, s14, v26
	v_mul_f32_e32 v27, s14, v27
	v_add3_u32 v24, v24, v32, s23
	v_bfe_u32 v32, v25, 16, 1
	v_fma_f32 v26, v26, v90, v10
	v_fma_f32 v27, v27, v91, v11
	v_lshrrev_b32_e32 v24, 16, v24
	v_add3_u32 v25, v25, v32, s23
	v_and_or_b32 v24, v25, s42, v24
	v_bfe_u32 v25, v26, 16, 1
	v_add3_u32 v25, v26, v25, s23
	v_bfe_u32 v26, v27, 16, 1
	v_lshrrev_b32_e32 v25, 16, v25
	v_add3_u32 v26, v27, v26, s23
	s_waitcnt vmcnt(18)
; #define P6_LD(bi, r) do { const GAS f32x4* xr_ = (const GAS f32x4*)(XOUT + ((size_t)p * 256 + wave * 32 + (r)) * DM) + lane2; _Pragma("unroll") for (int j = 0; j < 4; ++j) xq[bi][j] = xr_[64 * j]; } while (0)
; __device__ __forceinline__ unsigned f2bf(float f) { unsigned u = __builtin_bit_cast(unsigned, f); return (u + 0x7fffu + ((u >> 16) & 1u)) >> 16; }
; __device__ __forceinline__ unsigned pk2(float lo, float hi) { return f2bf(lo) | (f2bf(hi) << 16); }
; __global__ void __launch_bounds__(512, 2) hymba_fwd(Args args) {
;     ...
;             { f32x4 av[4], sv[4]; int lane2 = lane; asm volatile("" : "+v"(lane2));
; #pragma unroll
;               for (int j = 0; j < 4; ++j) { const int c0 = 4 * lane2 + 256 * j; sv[j] = *(const f32x4*)(sh2 + c0); av[j] = *(const f32x4*)(g2p + c0) * (1.0f + *(const f32x4*)(scl2 + c0)); }
;               f32x4 xq[4][4];
;     ...
;               P6_LD(0, 0); P6_LD(1, 1); P6_LD(2, 2); asm volatile("" ::: "memory");
; #pragma nounroll
;               for (int rr = 0; rr < 32; rr += 4) { const int r4 = (rr + 4 < 32) ? rr + 4 : 28;
;                   P6_LD(3, rr + 3); asm volatile("" ::: "memory"); P6_ST(0, rr); asm volatile("" ::: "memory");
;                   P6_LD(0, r4); asm volatile("" ::: "memory"); P6_ST(1, rr + 1); asm volatile("" ::: "memory");
;                   P6_LD(1, r4 + 1); asm volatile("" ::: "memory"); P6_ST(2, rr + 2); asm volatile("" ::: "memory");
;                   P6_LD(2, r4 + 2); asm volatile("" ::: "memory"); P6_ST(3, rr + 3); asm volatile("" ::: "memory"); }
	v_mul_f32_e32 v16, s14, v16
	v_mul_f32_e32 v17, s14, v17
	v_and_or_b32 v25, v26, s42, v25
	v_fma_f32 v16, v16, v96, v12
	v_fma_f32 v17, v17, v97, v13
	global_store_dwordx2 v[106:107], v[24:25], off offset:-512
	v_bfe_u32 v24, v16, 16, 1
	v_mul_f32_e32 v18, s14, v18
	v_mul_f32_e32 v19, s14, v19
	v_add3_u32 v16, v16, v24, s23
	v_bfe_u32 v24, v17, 16, 1
	v_fma_f32 v18, v18, v94, v14
	v_fma_f32 v19, v19, v95, v15
	v_lshrrev_b32_e32 v16, 16, v16
	v_add3_u32 v17, v17, v24, s23
	v_and_or_b32 v16, v17, s42, v16
	v_bfe_u32 v17, v18, 16, 1
	v_add3_u32 v17, v18, v17, s23
	v_bfe_u32 v18, v19, 16, 1
	v_lshrrev_b32_e32 v17, 16, v17
	v_add3_u32 v18, v19, v18, s23
	v_and_or_b32 v17, v18, s42, v17
	global_store_dwordx2 v[104:105], v[16:17], off offset:-4096
	v_lshl_add_u64 v[16:17], v[98:99], 0, s[12:13]
	v_readlane_b32 s12, v80, s58
	global_load_dwordx4 v[40:43], v[16:17], off
	global_load_dwordx4 v[32:35], v[16:17], off offset:1024
	global_load_dwordx4 v[24:27], v[16:17], off offset:2048
	s_nop 0
	global_load_dwordx4 v[16:19], v[16:17], off offset:3072
	s_waitcnt vmcnt(23)
	v_mul_f32_e32 v60, s12, v60
	v_mul_f32_e32 v61, s12, v61
	v_fma_f32 v60, v60, v84, v0
	v_fma_f32 v61, v61, v85, v1
	v_mul_f32_e32 v62, s12, v62
	v_mul_f32_e32 v63, s12, v63
	v_bfe_u32 v81, v60, 16, 1
	v_add3_u32 v60, v60, v81, s23
	v_bfe_u32 v81, v61, 16, 1
	v_fma_f32 v62, v62, v82, v2
	v_fma_f32 v63, v63, v83, v3
	v_lshrrev_b32_e32 v60, 16, v60
	v_add3_u32 v61, v61, v81, s23
	v_and_or_b32 v60, v61, s42, v60
	v_bfe_u32 v61, v62, 16, 1
	v_add3_u32 v61, v62, v61, s23
	v_bfe_u32 v62, v63, 16, 1
	v_lshrrev_b32_e32 v61, 16, v61
	v_add3_u32 v62, v63, v62, s23
	s_waitcnt vmcnt(22)
	v_mul_f32_e32 v56, s12, v56
	v_mul_f32_e32 v57, s12, v57
	v_and_or_b32 v61, v62, s42, v61
	v_fma_f32 v56, v56, v88, v4
	v_fma_f32 v57, v57, v89, v5
	global_store_dwordx2 v[104:105], v[60:61], off offset:-3584
	v_bfe_u32 v60, v56, 16, 1
	v_mul_f32_e32 v58, s12, v58
	v_mul_f32_e32 v59, s12, v59
	v_add3_u32 v56, v56, v60, s23
	v_bfe_u32 v60, v57, 16, 1
	v_fma_f32 v58, v58, v86, v6
	v_fma_f32 v59, v59, v87, v7
	v_lshrrev_b32_e32 v56, 16, v56
	v_add3_u32 v57, v57, v60, s23
	v_and_or_b32 v56, v57, s42, v56
	v_bfe_u32 v57, v58, 16, 1
	v_add3_u32 v57, v58, v57, s23
	v_bfe_u32 v58, v59, 16, 1
	v_lshrrev_b32_e32 v57, 16, v57
	v_add3_u32 v58, v59, v58, s23
	s_waitcnt vmcnt(22)
	v_mul_f32_e32 v52, s12, v52
	v_mul_f32_e32 v53, s12, v53
	v_and_or_b32 v57, v58, s42, v57
	v_fma_f32 v52, v52, v92, v8
	v_fma_f32 v53, v53, v93, v9
	global_store_dwordx2 v[104:105], v[56:57], off offset:-3072
	v_bfe_u32 v56, v52, 16, 1
	v_mul_f32_e32 v54, s12, v54
	v_mul_f32_e32 v55, s12, v55
	v_add3_u32 v52, v52, v56, s23
	v_bfe_u32 v56, v53, 16, 1
	v_pk_fma_f32 v[54:55], v[54:55], v[90:91], v[10:11]
	v_lshrrev_b32_e32 v52, 16, v52
	v_add3_u32 v53, v53, v56, s23
	v_and_or_b32 v52, v53, s42, v52
	v_bfe_u32 v53, v54, 16, 1
	v_add3_u32 v53, v54, v53, s23
	v_bfe_u32 v54, v55, 16, 1
	v_lshrrev_b32_e32 v53, 16, v53
	v_add3_u32 v54, v55, v54, s23
	s_waitcnt vmcnt(22)
	v_pk_mul_f32 v[44:45], s[12:13], v[44:45] op_sel_hi:[0,1]
	v_and_or_b32 v53, v54, s42, v53
	v_pk_fma_f32 v[44:45], v[44:45], v[96:97], v[12:13]
	global_store_dwordx2 v[104:105], v[52:53], off offset:-2560
	v_bfe_u32 v52, v44, 16, 1
	v_pk_mul_f32 v[46:47], s[12:13], v[46:47] op_sel_hi:[0,1]
	v_add3_u32 v44, v44, v52, s23
	v_bfe_u32 v52, v45, 16, 1
	v_pk_fma_f32 v[46:47], v[46:47], v[94:95], v[14:15]
	v_lshrrev_b32_e32 v44, 16, v44
	v_add3_u32 v45, v45, v52, s23
	v_and_or_b32 v44, v45, s42, v44
	v_bfe_u32 v45, v46, 16, 1
	v_add3_u32 v45, v46, v45, s23
	v_bfe_u32 v46, v47, 16, 1
	v_lshrrev_b32_e32 v45, 16, v45
	v_add3_u32 v46, v47, v46, s23
	v_and_or_b32 v45, v46, s42, v45
	global_store_dwordx2 v[104:105], v[44:45], off offset:-2048
	v_lshl_add_u64 v[44:45], v[98:99], 0, s[10:11]
	global_load_dwordx4 v[60:63], v[44:45], off
	global_load_dwordx4 v[56:59], v[44:45], off offset:1024
	global_load_dwordx4 v[52:55], v[44:45], off offset:2048
	s_nop 0
	global_load_dwordx4 v[44:47], v[44:45], off offset:3072
	v_readlane_b32 s10, v80, s43
	v_lshl_add_u64 v[102:103], v[102:103], 0, s[94:95]
	s_mov_b64 s[18:19], s[8:9]
	s_waitcnt vmcnt(27)
	v_pk_mul_f32 v[76:77], s[10:11], v[76:77] op_sel_hi:[0,1]
	v_pk_fma_f32 v[76:77], v[76:77], v[84:85], v[0:1]
	v_pk_mul_f32 v[78:79], s[10:11], v[78:79] op_sel_hi:[0,1]
	v_bfe_u32 v81, v76, 16, 1
	v_add3_u32 v76, v76, v81, s23
	v_bfe_u32 v81, v77, 16, 1
	v_pk_fma_f32 v[78:79], v[78:79], v[82:83], v[2:3]
	v_lshrrev_b32_e32 v76, 16, v76
	v_add3_u32 v77, v77, v81, s23
	v_and_or_b32 v76, v77, s42, v76
	v_bfe_u32 v77, v78, 16, 1
	v_add3_u32 v77, v78, v77, s23
	v_bfe_u32 v78, v79, 16, 1
	v_lshrrev_b32_e32 v77, 16, v77
	v_add3_u32 v78, v79, v78, s23
	s_waitcnt vmcnt(26)
	v_pk_mul_f32 v[72:73], s[10:11], v[72:73] op_sel_hi:[0,1]
	v_and_or_b32 v77, v78, s42, v77
	v_pk_fma_f32 v[72:73], v[72:73], v[88:89], v[4:5]
	global_store_dwordx2 v[104:105], v[76:77], off offset:-1536
	v_bfe_u32 v76, v72, 16, 1
	v_pk_mul_f32 v[74:75], s[10:11], v[74:75] op_sel_hi:[0,1]
	v_add3_u32 v72, v72, v76, s23
	v_bfe_u32 v76, v73, 16, 1
	v_pk_fma_f32 v[74:75], v[74:75], v[86:87], v[6:7]
	v_lshrrev_b32_e32 v72, 16, v72
	v_add3_u32 v73, v73, v76, s23
	v_and_or_b32 v72, v73, s42, v72
	v_bfe_u32 v73, v74, 16, 1
	v_add3_u32 v73, v74, v73, s23
	v_bfe_u32 v74, v75, 16, 1
	v_lshrrev_b32_e32 v73, 16, v73
	v_add3_u32 v74, v75, v74, s23
	s_waitcnt vmcnt(26)
	v_pk_mul_f32 v[68:69], s[10:11], v[68:69] op_sel_hi:[0,1]
	v_and_or_b32 v73, v74, s42, v73
	v_pk_fma_f32 v[68:69], v[68:69], v[92:93], v[8:9]
	global_store_dwordx2 v[104:105], v[72:73], off offset:-1024
	v_bfe_u32 v72, v68, 16, 1
	v_pk_mul_f32 v[70:71], s[10:11], v[70:71] op_sel_hi:[0,1]
	v_add3_u32 v68, v68, v72, s23
	v_bfe_u32 v72, v69, 16, 1
	v_pk_fma_f32 v[70:71], v[70:71], v[90:91], v[10:11]
	v_lshrrev_b32_e32 v68, 16, v68
	v_add3_u32 v69, v69, v72, s23
	v_and_or_b32 v68, v69, s42, v68
	v_bfe_u32 v69, v70, 16, 1
	v_add3_u32 v69, v70, v69, s23
	v_bfe_u32 v70, v71, 16, 1
	v_lshrrev_b32_e32 v69, 16, v69
	v_add3_u32 v70, v71, v70, s23
	s_waitcnt vmcnt(26)
	v_pk_mul_f32 v[64:65], s[10:11], v[64:65] op_sel_hi:[0,1]
	v_and_or_b32 v69, v70, s42, v69
	v_pk_fma_f32 v[64:65], v[64:65], v[96:97], v[12:13]
	global_store_dwordx2 v[104:105], v[68:69], off offset:-512
	v_bfe_u32 v68, v64, 16, 1
	v_pk_mul_f32 v[66:67], s[10:11], v[66:67] op_sel_hi:[0,1]
	v_add3_u32 v64, v64, v68, s23
	v_bfe_u32 v68, v65, 16, 1
	v_pk_fma_f32 v[66:67], v[66:67], v[94:95], v[14:15]
	v_lshrrev_b32_e32 v64, 16, v64
	v_add3_u32 v65, v65, v68, s23
	v_and_or_b32 v64, v65, s42, v64
	v_bfe_u32 v65, v66, 16, 1
	v_add3_u32 v65, v66, v65, s23
	v_bfe_u32 v66, v67, 16, 1
	v_lshrrev_b32_e32 v65, 16, v65
	v_add3_u32 v66, v67, v66, s23
	v_and_or_b32 v65, v66, s42, v65
	global_store_dwordx2 v[104:105], v[64:65], off
	s_mov_b32 s16, s17
	s_cbranch_scc0 .LBB0_877
; __device__ __forceinline__ int lane_id_v() { int l; asm volatile("v_mbcnt_lo_u32_b32 %0, -1, 0\n\tv_mbcnt_hi_u32_b32 %0, -1, %0" : "=v"(l)); return l; }
; __global__ void __launch_bounds__(512, 2) hymba_fwd(Args args) {
;     ...
;             __syncthreads();
;             const int tidB = wave * 64 + lane_id_v();
;             if (tidB < 32) lbase[tidB] = (int)__hip_atomic_fetch_add(ECNT + tidB, (unsigned)lcnt[tidB], RLX_AGENT);
	s_barrier
	v_mbcnt_lo_u32_b32 v3, -1, 0
	v_mbcnt_hi_u32_b32 v3, -1, v3
	s_nop 0
	v_add_u32_e32 v0, s56, v3
	v_cmp_gt_i32_e32 vcc, 32, v0
	v_lshl_add_u32 v2, v0, 2, 0
	s_and_saveexec_b64 s[2:3], vcc
	s_cbranch_execz .LBB0_865
	v_readlane_b32 s8, v248, 16
	v_add_u32_e32 v7, 0x25800, v2
	v_ashrrev_i32_e32 v1, 31, v0
	v_readlane_b32 s9, v248, 17
	v_add_u32_e32 v6, 0x25880, v2
	s_nop 0
	v_lshl_add_u64 v[4:5], v[0:1], 2, s[8:9]
	ds_read_b32 v1, v7
	s_waitcnt lgkmcnt(0)
	global_atomic_add v1, v[4:5], v1, off sc0
	s_waitcnt vmcnt(0)
	ds_write_b32 v6, v1
	s_branch .LBB0_865
